# LDS round-trip batching: router rank rows read with 8 ds_read_b128 in flight (was 8 serial round trips x2); GLA unit tail LDS->global copy reads batched
# baseline (speedup 1.0000x reference)
.LBB0_287:
	s_or_b64 exec, exec, s[14:15]
	s_waitcnt lgkmcnt(0)
	s_barrier
	v_readlane_b32 s11, v254, 45
	ds_read_b128 v[6:9], v129
	s_add_u32 s14, s11, s19
	v_readlane_b32 s11, v254, 46
	s_addc_u32 s15, s11, 0
	v_lshl_add_u64 v[2:3], s[14:15], 0, v[2:3]
	v_lshl_add_u64 v[2:3], v[2:3], 0, v[34:35]
	s_waitcnt lgkmcnt(0)
	global_store_dwordx4 v[2:3], v[6:9], off
	ds_read_b128 v[6:9], v130
	v_lshl_add_u64 v[2:3], s[14:15], 0, v[4:5]
	v_lshl_add_u64 v[2:3], v[2:3], 0, v[34:35]
	v_add_u32_e32 v63, v131, v133
	v_readlane_b32 s14, v255, 4
	s_waitcnt lgkmcnt(0)
	global_store_dwordx4 v[2:3], v[6:9], off
	ds_read_b128 v[2:5], v63 offset:17408
	ds_read_b128 v[18:21], v63 offset:17440
	ds_read_b128 v[22:25], v132
	ds_read_b128 v[26:29], v132 offset:32
	s_waitcnt lgkmcnt(1)
	v_mfma_f32_32x32x16_bf16 v[2:17], v[2:5], v[22:25], 0
	v_readlane_b32 s15, v255, 5
	s_lshl_b32 s11, s18, 8
	s_lshl_b32 s8, s8, 1
	s_waitcnt lgkmcnt(0)
	v_mfma_f32_32x32x16_bf16 v[2:17], v[18:21], v[26:29], v[2:17]
	ds_read_b128 v[18:21], v63 offset:17472
	ds_read_b128 v[30:33], v132 offset:64
	s_waitcnt lgkmcnt(0)
	v_mfma_f32_32x32x16_bf16 v[2:17], v[18:21], v[30:33], v[2:17]
	ds_read_b128 v[18:21], v63 offset:17504
	ds_read_b128 v[66:69], v132 offset:96
	s_waitcnt lgkmcnt(0)
	v_mfma_f32_32x32x16_bf16 v[2:17], v[18:21], v[66:69], v[2:17]
	ds_read_b128 v[18:21], v63 offset:17536
	ds_read_b128 v[150:153], v132 offset:128
	s_waitcnt lgkmcnt(0)
	v_mfma_f32_32x32x16_bf16 v[2:17], v[18:21], v[150:153], v[2:17]
	ds_read_b128 v[18:21], v63 offset:17568
	ds_read_b128 v[154:157], v132 offset:160
	s_waitcnt lgkmcnt(0)
	v_mfma_f32_32x32x16_bf16 v[2:17], v[18:21], v[154:157], v[2:17]
	ds_read_b128 v[18:21], v63 offset:17600
	ds_read_b128 v[158:161], v132 offset:192
	s_waitcnt lgkmcnt(0)
	v_mfma_f32_32x32x16_bf16 v[2:17], v[18:21], v[158:161], v[2:17]
	ds_read_b128 v[18:21], v63 offset:17632
	ds_read_b128 v[162:165], v132 offset:224
	s_waitcnt lgkmcnt(0)
	v_mfma_f32_32x32x16_bf16 v[2:17], v[18:21], v[162:165], v[2:17]
	s_nop 11
	v_cndmask_b32_e64 v18, v2, 0, s[14:15]
	v_readlane_b32 s14, v255, 6
	v_readlane_b32 s15, v255, 7
	v_cndmask_b32_e64 v149, v18, v2, s[12:13]
	v_cndmask_b32_e64 v168, 0, v3, s[12:13]
	v_cndmask_b32_e64 v169, v4, 0, s[14:15]
	v_readlane_b32 s14, v255, 8
	v_readlane_b32 s15, v255, 9
	ds_read_b128 v[18:21], v63 offset:26144
	v_cndmask_b32_e64 v172, v7, 0, s[20:21]
	v_cndmask_b32_e64 v170, v5, 0, s[14:15]
	ds_read_b128 v[2:5], v63 offset:26112
	v_readlane_b32 s14, v255, 10
	v_readlane_b32 s15, v255, 11
	v_cndmask_b32_e64 v173, v8, 0, s[22:23]
	v_cndmask_b32_e64 v174, v9, 0, s[24:25]
	v_cndmask_b32_e64 v171, v6, 0, s[14:15]
	v_cndmask_b32_e64 v175, v10, 0, s[26:27]
	v_cndmask_b32_e64 v176, v11, 0, s[28:29]
	v_cndmask_b32_e64 v177, v12, 0, s[30:31]
	v_cndmask_b32_e64 v178, v13, 0, s[34:35]
	v_cndmask_b32_e64 v179, v14, 0, s[2:3]
	v_cndmask_b32_e64 v180, v15, 0, s[38:39]
	v_cndmask_b32_e64 v181, v16, 0, s[40:41]
	v_cndmask_b32_e64 v182, v17, 0, s[42:43]
	s_waitcnt lgkmcnt(0)
	v_mfma_f32_32x32x16_bf16 v[2:17], v[2:5], v[22:25], 0
	v_readlane_b32 s14, v254, 49
	v_cvt_pk_bf16_f32 v22, v175, v176
	v_cvt_pk_bf16_f32 v23, v177, v178
	v_cvt_pk_bf16_f32 v24, v179, v180
	v_cvt_pk_bf16_f32 v25, v181, v182
	v_mfma_f32_32x32x16_bf16 v[2:17], v[18:21], v[26:29], v[2:17]
	ds_read_b128 v[18:21], v63 offset:26176
	s_waitcnt lgkmcnt(0)
	v_mfma_f32_32x32x16_bf16 v[2:17], v[18:21], v[30:33], v[2:17]
	ds_read_b128 v[18:21], v63 offset:26208
	s_waitcnt lgkmcnt(0)
	v_mfma_f32_32x32x16_bf16 v[2:17], v[18:21], v[66:69], v[2:17]
	ds_read_b128 v[18:21], v63 offset:26240
	v_lshl_add_u64 v[68:69], v[40:41], 0, s[8:9]
	v_lshlrev_b64 v[66:67], 15, v[64:65]
	v_lshl_add_u64 v[66:67], v[58:59], 0, v[66:67]
	v_lshlrev_b64 v[64:65], 16, v[64:65]
	s_waitcnt lgkmcnt(0)
	v_mfma_f32_32x32x16_bf16 v[2:17], v[18:21], v[150:153], v[2:17]
	ds_read_b128 v[18:21], v63 offset:26272
	s_waitcnt lgkmcnt(0)
	v_mfma_f32_32x32x16_bf16 v[2:17], v[18:21], v[154:157], v[2:17]
	ds_read_b128 v[18:21], v63 offset:26304
	s_waitcnt lgkmcnt(0)
	v_mfma_f32_32x32x16_bf16 v[2:17], v[18:21], v[158:161], v[2:17]
	ds_read_b128 v[18:21], v63 offset:26336
	s_waitcnt lgkmcnt(0)
	v_mfma_f32_32x32x16_bf16 v[2:17], v[18:21], v[162:165], v[2:17]
	v_or_b32_e32 v163, s11, v167
	v_cvt_pk_bf16_f32 v19, v169, v170
	v_cvt_pk_bf16_f32 v20, v171, v172
	v_cvt_pk_bf16_f32 v21, v173, v174
	s_nop 7
	v_cndmask_b32_e64 v18, v2, 0, s[44:45]
	v_cndmask_b32_e64 v30, v18, v2, s[46:47]
	v_add_u32_e32 v2, s14, v163
	v_cndmask_b32_e64 v31, 0, v3, s[46:47]
	v_ashrrev_i32_e32 v3, 31, v2
	v_lshlrev_b64 v[2:3], 12, v[2:3]
	v_lshl_add_u64 v[152:153], v[68:69], 0, v[2:3]
	v_cndmask_b32_e64 v32, v4, 0, s[50:51]
	v_cndmask_b32_e64 v33, v5, 0, s[52:53]
	global_load_dwordx2 v[2:3], v[152:153], off
	global_load_dwordx2 v[4:5], v[152:153], off offset:16
	global_load_dwordx2 v[26:27], v[152:153], off offset:32
	global_load_dwordx2 v[28:29], v[152:153], off offset:48
	global_load_dwordx2 v[198:199], v[152:153], off offset:64
	global_load_dwordx2 v[200:201], v[152:153], off offset:80
	global_load_dwordx2 v[202:203], v[152:153], off offset:96
	global_load_dwordx2 v[204:205], v[152:153], off offset:112
	v_readlane_b32 s14, v254, 51
	s_nop 1
	v_add_u32_e32 v212, s14, v163
	v_ashrrev_i32_e32 v213, 31, v212
	v_lshlrev_b64 v[212:213], 12, v[212:213]
	v_lshl_add_u64 v[230:231], v[68:69], 0, v[212:213]
	global_load_dwordx2 v[206:207], v[230:231], off
	global_load_dwordx2 v[208:209], v[230:231], off offset:16
	global_load_dwordx2 v[218:219], v[230:231], off offset:32
	global_load_dwordx2 v[220:221], v[230:231], off offset:48
	global_load_dwordx2 v[222:223], v[230:231], off offset:64
	global_load_dwordx2 v[224:225], v[230:231], off offset:80
	global_load_dwordx2 v[226:227], v[230:231], off offset:96
	global_load_dwordx2 v[228:229], v[230:231], off offset:112
	v_add_u32_e32 v212, s11, v134
	v_ashrrev_i32_e32 v213, 31, v212
	v_lshlrev_b64 v[212:213], 12, v[212:213]
	v_lshl_add_u64 v[232:233], s[6:7], 0, v[212:213]
	v_lshl_add_u64 v[232:233], v[232:233], 0, s[8:9]
	v_mov_b32_e32 v234, v62
	v_mov_b32_e32 v235, v35
	v_lshl_add_u64 v[232:233], v[232:233], 0, v[234:235]
	global_load_dwordx4 v[238:241], v[232:233], off
	global_load_dwordx4 v[242:245], v[232:233], off offset:32
	global_load_dwordx4 v[246:249], v[232:233], off offset:64
	global_load_dwordx4 v[250:253], v[232:233], off offset:96
	v_cvt_pk_bf16_f32 v18, v149, v168
	v_cndmask_b32_e64 v63, v6, 0, s[54:55]
	v_cndmask_b32_e64 v150, v7, 0, s[78:79]
	v_cndmask_b32_e64 v151, v8, 0, s[96:97]
	v_cndmask_b32_e64 v154, v9, 0, s[0:1]
	v_cndmask_b32_e64 v155, v10, 0, s[76:77]
	v_cndmask_b32_e64 v156, v11, 0, s[4:5]
	v_cndmask_b32_e64 v157, v12, 0, s[64:65]
	v_cndmask_b32_e64 v158, v13, 0, s[66:67]
	v_cndmask_b32_e64 v159, v14, 0, s[68:69]
	v_cndmask_b32_e64 v160, v15, 0, s[70:71]
	v_cndmask_b32_e64 v161, v16, 0, s[72:73]
	v_cndmask_b32_e64 v162, v17, 0, s[74:75]
	s_waitcnt vmcnt(18)
	v_mfma_f32_32x32x16_bf16 v[2:17], v[2:5], v[18:21], 0
	s_waitcnt vmcnt(16)
	v_mfma_f32_32x32x16_bf16 v[2:17], v[26:29], v[22:25], v[2:17]
	v_cvt_pk_bf16_f32 v26, v30, v31
	v_cvt_pk_bf16_f32 v27, v32, v33
	v_cvt_pk_bf16_f32 v28, v63, v150
	v_cvt_pk_bf16_f32 v29, v151, v154
	v_mov_b32_e32 v63, v35
	s_waitcnt vmcnt(14)
	v_mfma_f32_32x32x16_bf16 v[2:17], v[198:201], v[26:29], v[2:17]
	v_cvt_pk_bf16_f32 v30, v155, v156
	v_cvt_pk_bf16_f32 v31, v157, v158
	v_cvt_pk_bf16_f32 v32, v159, v160
	v_cvt_pk_bf16_f32 v33, v161, v162
	s_waitcnt vmcnt(12)
	s_nop 0
	v_mfma_f32_32x32x16_bf16 v[2:17], v[202:205], v[30:33], v[2:17]
	s_nop 11
	v_cvt_pk_bf16_f32 v2, v2, v3
	v_cvt_pk_bf16_f32 v3, v4, v5
	v_cvt_pk_bf16_f32 v4, v6, v7
	v_cvt_pk_bf16_f32 v5, v8, v9
	global_store_dwordx4 v[66:67], v[2:5], off
	s_nop 1
	v_cvt_pk_bf16_f32 v2, v10, v11
	v_cvt_pk_bf16_f32 v3, v12, v13
	v_cvt_pk_bf16_f32 v4, v14, v15
	v_cvt_pk_bf16_f32 v5, v16, v17
	global_store_dwordx4 v[66:67], v[2:5], off offset:1024
	s_nop 1
	s_waitcnt vmcnt(12)
	v_mfma_f32_32x32x16_bf16 v[2:17], v[206:209], v[18:21], 0
	s_waitcnt vmcnt(10)
	v_mfma_f32_32x32x16_bf16 v[2:17], v[218:221], v[22:25], v[2:17]
	s_waitcnt vmcnt(8)
	v_mfma_f32_32x32x16_bf16 v[2:17], v[222:225], v[26:29], v[2:17]
	s_waitcnt vmcnt(6)
	v_mfma_f32_32x32x16_bf16 v[2:17], v[226:229], v[30:33], v[2:17]
	s_nop 11
	v_cvt_pk_bf16_f32 v2, v2, v3
	v_cvt_pk_bf16_f32 v3, v4, v5
	v_cvt_pk_bf16_f32 v4, v6, v7
	v_cvt_pk_bf16_f32 v5, v8, v9
	global_store_dwordx4 v[66:67], v[2:5], off offset:2048
	s_nop 1
	v_cvt_pk_bf16_f32 v2, v10, v11
	v_cvt_pk_bf16_f32 v3, v12, v13
	v_cvt_pk_bf16_f32 v4, v14, v15
	v_cvt_pk_bf16_f32 v5, v16, v17
	global_store_dwordx4 v[66:67], v[2:5], off offset:3072
	s_nop 1
	v_add_u32_e32 v63, v131, v137
	ds_read_b128 v[2:5], v63 offset:34816
	ds_read_b128 v[66:69], v63 offset:34848
	v_readlane_b32 s8, v254, 53
	s_waitcnt vmcnt(7) lgkmcnt(1)
	v_mfma_f32_32x32x16_bf16 v[2:17], v[238:241], v[2:5], 0
	s_waitcnt vmcnt(6) lgkmcnt(0)
	v_mfma_f32_32x32x16_bf16 v[2:17], v[242:245], v[66:69], v[2:17]
	ds_read_b128 v[66:69], v63 offset:34880
	s_waitcnt vmcnt(5) lgkmcnt(0)
	v_mfma_f32_32x32x16_bf16 v[2:17], v[246:249], v[66:69], v[2:17]
	ds_read_b128 v[66:69], v63 offset:34912
	s_waitcnt vmcnt(4) lgkmcnt(0)
	v_mfma_f32_32x32x16_bf16 v[2:17], v[250:253], v[66:69], v[2:17]
	v_add_u32_e32 v66, s8, v135
	v_readlane_b32 s8, v254, 54
	s_nop 1
	v_add_u32_e32 v67, s8, v135
	v_readlane_b32 s8, v254, 55
	s_nop 5
	v_cvt_pk_bf16_f32 v2, v2, s0
	ds_write_b16 v136, v2 offset:59392
	v_cvt_pk_bf16_f32 v2, v3, s0
	ds_write_b16 v136, v2 offset:59648
	v_cvt_pk_bf16_f32 v2, v4, s0
	ds_write_b16 v136, v2 offset:59904
	v_cvt_pk_bf16_f32 v2, v5, s0
	ds_write_b16 v136, v2 offset:60160
	v_cvt_pk_bf16_f32 v2, v6, s0
	ds_write_b16 v136, v2 offset:61440
	v_cvt_pk_bf16_f32 v2, v7, s0
	ds_write_b16 v136, v2 offset:61696
	v_cvt_pk_bf16_f32 v2, v8, s0
	ds_write_b16 v136, v2 offset:61952
	v_cvt_pk_bf16_f32 v2, v9, s0
	ds_write_b16 v136, v2 offset:62208
	v_cvt_pk_bf16_f32 v2, v10, s0
	ds_write_b16 v136, v2 offset:63488
	v_cvt_pk_bf16_f32 v2, v11, s0
	ds_write_b16 v136, v2 offset:63744
	v_cvt_pk_bf16_f32 v2, v12, s0
	ds_write_b16 v136, v2 offset:64000
	v_cvt_pk_bf16_f32 v2, v13, s0
	ds_write_b16 v136, v2 offset:64256
	v_cvt_pk_bf16_f32 v2, v14, s0
	ds_write_b16 v66, v2 offset:59392
	v_cvt_pk_bf16_f32 v2, v15, s0
	ds_write_b16 v67, v2 offset:59392
	v_cvt_pk_bf16_f32 v2, v16, s0
	v_add_u32_e32 v68, s8, v135
	v_readlane_b32 s8, v254, 57
	ds_write_b16 v68, v2 offset:59392
	v_cvt_pk_bf16_f32 v2, v17, s0
	v_add_u32_e32 v69, s8, v135
	ds_write_b16 v69, v2 offset:59392
	ds_read_b128 v[2:5], v63 offset:39424
	ds_read_b128 v[150:153], v63 offset:39456
	s_waitcnt lgkmcnt(1)
	v_mfma_f32_32x32x16_bf16 v[2:17], v[238:241], v[2:5], 0
	v_readlane_b32 s8, v254, 36
	s_add_i32 s10, s10, s8
	v_readlane_b32 s8, v255, 12
	s_add_i32 s16, s16, s8
	v_readlane_b32 s8, v255, 13
	s_add_i32 s17, s17, s8
	s_cmpk_gt_i32 s10, 0x1ff
	s_waitcnt lgkmcnt(0)
	v_mfma_f32_32x32x16_bf16 v[2:17], v[242:245], v[150:153], v[2:17]
	ds_read_b128 v[150:153], v63 offset:39488
	s_waitcnt lgkmcnt(0)
	v_mfma_f32_32x32x16_bf16 v[2:17], v[246:249], v[150:153], v[2:17]
	ds_read_b128 v[150:153], v63 offset:39520
	s_waitcnt lgkmcnt(0)
	v_mfma_f32_32x32x16_bf16 v[2:17], v[250:253], v[150:153], v[2:17]
	s_nop 11
	v_cvt_pk_bf16_f32 v2, v2, s0
	ds_write_b16 v136, v2 offset:59456
	v_cvt_pk_bf16_f32 v2, v3, s0
	ds_write_b16 v136, v2 offset:59712
	v_cvt_pk_bf16_f32 v2, v4, s0
	ds_write_b16 v136, v2 offset:59968
	v_cvt_pk_bf16_f32 v2, v5, s0
	ds_write_b16 v136, v2 offset:60224
	v_cvt_pk_bf16_f32 v2, v6, s0
	ds_write_b16 v136, v2 offset:61504
	v_cvt_pk_bf16_f32 v2, v7, s0
	ds_write_b16 v136, v2 offset:61760
	v_cvt_pk_bf16_f32 v2, v8, s0
	ds_write_b16 v136, v2 offset:62016
	v_cvt_pk_bf16_f32 v2, v9, s0
	ds_write_b16 v136, v2 offset:62272
	v_cvt_pk_bf16_f32 v2, v10, s0
	ds_write_b16 v136, v2 offset:63552
	v_cvt_pk_bf16_f32 v2, v11, s0
	ds_write_b16 v136, v2 offset:63808
	v_cvt_pk_bf16_f32 v2, v12, s0
	ds_write_b16 v136, v2 offset:64064
	v_cvt_pk_bf16_f32 v2, v13, s0
	ds_write_b16 v136, v2 offset:64320
	v_cvt_pk_bf16_f32 v2, v14, s0
	ds_write_b16 v66, v2 offset:59456
	v_cvt_pk_bf16_f32 v2, v15, s0
	ds_write_b16 v67, v2 offset:59456
	v_cvt_pk_bf16_f32 v2, v16, s0
	ds_write_b16 v68, v2 offset:59456
	v_cvt_pk_bf16_f32 v2, v17, s0
	ds_write_b16 v69, v2 offset:59456
	ds_read_b128 v[2:5], v63 offset:44032
	ds_read_b128 v[150:153], v63 offset:44064
	s_waitcnt lgkmcnt(1)
	v_mfma_f32_32x32x16_bf16 v[2:17], v[238:241], v[2:5], 0
	s_waitcnt lgkmcnt(0)
	v_mfma_f32_32x32x16_bf16 v[2:17], v[242:245], v[150:153], v[2:17]
	ds_read_b128 v[150:153], v63 offset:44096
	s_waitcnt lgkmcnt(0)
	v_mfma_f32_32x32x16_bf16 v[2:17], v[246:249], v[150:153], v[2:17]
	ds_read_b128 v[150:153], v63 offset:44128
	s_waitcnt lgkmcnt(0)
	v_mfma_f32_32x32x16_bf16 v[2:17], v[250:253], v[150:153], v[2:17]
	s_nop 11
	v_cvt_pk_bf16_f32 v2, v2, s0
	ds_write_b16 v136, v2 offset:59520
	v_cvt_pk_bf16_f32 v2, v3, s0
	ds_write_b16 v136, v2 offset:59776
	v_cvt_pk_bf16_f32 v2, v4, s0
	ds_write_b16 v136, v2 offset:60032
	v_cvt_pk_bf16_f32 v2, v5, s0
	ds_write_b16 v136, v2 offset:60288
	v_cvt_pk_bf16_f32 v2, v6, s0
	ds_write_b16 v136, v2 offset:61568
	v_cvt_pk_bf16_f32 v2, v7, s0
	ds_write_b16 v136, v2 offset:61824
	v_cvt_pk_bf16_f32 v2, v8, s0
	ds_write_b16 v136, v2 offset:62080
	v_cvt_pk_bf16_f32 v2, v9, s0
	ds_write_b16 v136, v2 offset:62336
	v_cvt_pk_bf16_f32 v2, v10, s0
	ds_write_b16 v136, v2 offset:63616
	v_cvt_pk_bf16_f32 v2, v11, s0
	ds_write_b16 v136, v2 offset:63872
	v_cvt_pk_bf16_f32 v2, v12, s0
	ds_write_b16 v136, v2 offset:64128
	v_cvt_pk_bf16_f32 v2, v13, s0
	ds_write_b16 v136, v2 offset:64384
	v_cvt_pk_bf16_f32 v2, v14, s0
	ds_write_b16 v66, v2 offset:59520
	v_cvt_pk_bf16_f32 v2, v15, s0
	ds_write_b16 v67, v2 offset:59520
	v_cvt_pk_bf16_f32 v2, v16, s0
	ds_write_b16 v68, v2 offset:59520
	v_cvt_pk_bf16_f32 v2, v17, s0
	ds_write_b16 v69, v2 offset:59520
	ds_read_b128 v[2:5], v63 offset:48640
	ds_read_b128 v[150:153], v63 offset:48672
	s_waitcnt lgkmcnt(1)
	v_mfma_f32_32x32x16_bf16 v[2:17], v[238:241], v[2:5], 0
	ds_read_b128 v[26:29], v63 offset:48704
	s_waitcnt lgkmcnt(1)
	v_mfma_f32_32x32x16_bf16 v[2:17], v[242:245], v[150:153], v[2:17]
	s_waitcnt lgkmcnt(0)
	v_mfma_f32_32x32x16_bf16 v[2:17], v[246:249], v[26:29], v[2:17]
	ds_read_b128 v[22:25], v63 offset:48736
	s_waitcnt lgkmcnt(0)
	v_mfma_f32_32x32x16_bf16 v[2:17], v[250:253], v[22:25], v[2:17]
	s_nop 11
	v_cvt_pk_bf16_f32 v2, v2, s0
	ds_write_b16 v136, v2 offset:59584
	v_cvt_pk_bf16_f32 v2, v3, s0
	ds_write_b16 v136, v2 offset:59840
	v_cvt_pk_bf16_f32 v2, v4, s0
	ds_write_b16 v136, v2 offset:60096
	v_cvt_pk_bf16_f32 v2, v5, s0
	ds_write_b16 v136, v2 offset:60352
	v_cvt_pk_bf16_f32 v2, v6, s0
	ds_write_b16 v136, v2 offset:61632
	v_cvt_pk_bf16_f32 v2, v7, s0
	ds_write_b16 v136, v2 offset:61888
	v_cvt_pk_bf16_f32 v2, v8, s0
	ds_write_b16 v136, v2 offset:62144
	v_cvt_pk_bf16_f32 v2, v9, s0
	ds_write_b16 v136, v2 offset:62400
	v_cvt_pk_bf16_f32 v2, v10, s0
	ds_write_b16 v136, v2 offset:63680
	v_cvt_pk_bf16_f32 v2, v11, s0
	ds_write_b16 v136, v2 offset:63936
	v_cvt_pk_bf16_f32 v2, v12, s0
	ds_write_b16 v136, v2 offset:64192
	v_cvt_pk_bf16_f32 v2, v13, s0
	ds_write_b16 v136, v2 offset:64448
	v_cvt_pk_bf16_f32 v2, v14, s0
	ds_write_b16 v66, v2 offset:59584
	v_cvt_pk_bf16_f32 v2, v15, s0
	ds_write_b16 v67, v2 offset:59584
	v_cvt_pk_bf16_f32 v2, v16, s0
	ds_write_b16 v68, v2 offset:59584
	v_cvt_pk_bf16_f32 v2, v17, s0
	ds_write_b16 v69, v2 offset:59584
	s_waitcnt lgkmcnt(0)
	v_add_u32_e32 v4, v70, v138
	ds_read_b128 v[198:201], v4 offset:59392
	v_add_u32_e32 v4, v70, v139
	ds_read_b128 v[202:205], v4 offset:59392
	v_add_u32_e32 v4, v70, v140
	ds_read_b128 v[206:209], v4 offset:59392
	v_add_u32_e32 v4, v70, v141
	ds_read_b128 v[218:221], v4 offset:59392
	v_add_u32_e32 v4, v70, v143
	ds_read_b128 v[222:225], v4 offset:59392
	v_add_u32_e32 v4, v70, v144
	ds_read_b128 v[226:229], v4 offset:59392
	v_add_u32_e32 v4, v70, v145
	ds_read_b128 v[230:233], v4 offset:59392
	v_add_u32_e32 v4, v70, v146
	ds_read_b128 v[238:241], v4 offset:59392
	v_lshl_add_u64 v[2:3], v[38:39], 0, v[64:65]
	v_lshl_add_u64 v[8:9], v[2:3], 0, v[42:43]
	s_waitcnt lgkmcnt(7)
	global_store_dwordx4 v[8:9], v[198:201], off
	v_lshl_add_u64 v[8:9], v[2:3], 0, v[44:45]
	s_waitcnt lgkmcnt(6)
	global_store_dwordx4 v[8:9], v[202:205], off
	v_lshl_add_u64 v[8:9], v[2:3], 0, v[46:47]
	s_waitcnt lgkmcnt(5)
	global_store_dwordx4 v[8:9], v[206:209], off
	v_lshl_add_u64 v[8:9], v[2:3], 0, v[48:49]
	s_waitcnt lgkmcnt(4)
	global_store_dwordx4 v[8:9], v[218:221], off
	v_lshl_add_u64 v[8:9], v[2:3], 0, v[50:51]
	s_waitcnt lgkmcnt(3)
	global_store_dwordx4 v[8:9], v[222:225], off
	v_lshl_add_u64 v[8:9], v[2:3], 0, v[52:53]
	s_waitcnt lgkmcnt(2)
	global_store_dwordx4 v[8:9], v[226:229], off
	v_lshl_add_u64 v[8:9], v[2:3], 0, v[54:55]
	s_waitcnt lgkmcnt(1)
	global_store_dwordx4 v[8:9], v[230:233], off
	v_lshl_add_u64 v[2:3], v[2:3], 0, v[56:57]
	s_waitcnt lgkmcnt(0)
	global_store_dwordx4 v[2:3], v[238:241], off
	s_barrier
	s_cbranch_scc1 .LBB0_294

.LBB0_837:
	s_or_b64 exec, exec, s[8:9]
	v_add_u32_e32 v10, 0x800, v93
	ds_write2_b32 v10, v6, v2 offset1:16
	ds_write2_b32 v10, v7, v3 offset0:32 offset1:48
	ds_write2_b32 v10, v8, v4 offset0:64 offset1:80
	ds_write2_b32 v10, v9, v5 offset0:96 offset1:112
	v_add_u32_e32 v6, 0x8000, v36
	s_waitcnt lgkmcnt(0)
	s_barrier
	ds_read2_b32 v[2:3], v6 offset1:32
	v_add_u32_e32 v4, v35, v37
	ds_read_b32 v4, v4
	ds_read_b32 v7, v74
	ds_read_b32 v10, v75
	ds_read_b32 v11, v76
	ds_read_b32 v12, v77
	ds_read_b32 v13, v78
	ds_read_b32 v14, v79
	ds_read_b32 v15, v80
	s_waitcnt lgkmcnt(7)
	v_add_f32_e32 v8, 0, v4
	ds_read2_b32 v[4:5], v6 offset0:64 offset1:96
	v_add_f32_e32 v2, 0, v2
	v_add_f32_e32 v16, v2, v3
	ds_read2_b32 v[2:3], v6 offset0:128 offset1:160
	s_waitcnt lgkmcnt(8)
	v_add_f32_e32 v7, v8, v7
	ds_read2_b32 v[8:9], v6 offset0:192 offset1:224
	s_waitcnt lgkmcnt(2)
	v_add_f32_e32 v4, v16, v4
	v_add_f32_e32 v4, v4, v5
	s_waitcnt lgkmcnt(1)
	v_add_f32_e32 v2, v4, v2
	v_add_f32_e32 v2, v2, v3
	s_waitcnt lgkmcnt(0)
	v_add_f32_e32 v2, v2, v8
	v_add_f32_e32 v2, v2, v9
	v_fmamk_f32 v2, v2, 0x3a000000, v81
	v_mul_f32_e32 v3, 0x4f800000, v2
	v_cmp_gt_f32_e32 vcc, s26, v2
	v_add_f32_e32 v4, v7, v10
	v_add_f32_e32 v4, v4, v11
	v_cndmask_b32_e32 v2, v2, v3, vcc
	v_sqrt_f32_e32 v3, v2
	v_add_f32_e32 v4, v4, v12
	v_add_f32_e32 v4, v4, v13
	v_add_f32_e32 v4, v4, v14
	v_add_u32_e32 v5, -1, v3
	v_fma_f32 v7, -v5, v3, v2
	v_cmp_ge_f32_e64 s[8:9], 0, v7
	v_add_u32_e32 v7, 1, v3
	v_add_f32_e32 v4, v4, v15
	v_cndmask_b32_e64 v5, v3, v5, s[8:9]
	v_fma_f32 v3, -v7, v3, v2
	v_cmp_lt_f32_e64 s[8:9], 0, v3
	v_mov_b32_e32 v10, 1
	s_nop 0
	v_cndmask_b32_e64 v3, v5, v7, s[8:9]
	v_mul_f32_e32 v5, 0x37800000, v3
	v_cndmask_b32_e32 v3, v3, v5, vcc
	v_cmp_class_f32_e32 vcc, v2, v82
	s_nop 1
	v_cndmask_b32_e32 v2, v3, v2, vcc
	v_div_scale_f32 v3, s[8:9], v2, v2, 1.0
	v_rcp_f32_e32 v5, v3
	s_nop 0
	v_fma_f32 v7, -v3, v5, 1.0
	v_fmac_f32_e32 v5, v7, v5
	v_div_scale_f32 v7, vcc, 1.0, v2, 1.0
	v_mul_f32_e32 v8, v7, v5
	v_fma_f32 v9, -v3, v8, v7
	v_fmac_f32_e32 v8, v9, v5
	v_fma_f32 v3, -v3, v8, v7
	v_div_fmas_f32 v3, v3, v5, v8
	v_div_fixup_f32 v7, v3, v2, 1.0
	v_fma_f32 v2, v4, v7, v56
	v_cmp_o_f32_e32 vcc, v2, v2
	v_mov_b32_e32 v9, 1
	s_nop 0
	v_cndmask_b32_e32 v8, v94, v2, vcc
	ds_write_b32 v71, v8 offset:36864
	s_waitcnt lgkmcnt(0)
	ds_read_b128 v[198:201], v20 offset:36864
	ds_read_b128 v[202:205], v20 offset:36880
	ds_read_b128 v[206:209], v20 offset:36896
	ds_read_b128 v[218:221], v20 offset:36912
	ds_read_b128 v[222:225], v20 offset:36928
	ds_read_b128 v[226:229], v20 offset:36944
	ds_read_b128 v[230:233], v20 offset:36960
	ds_read_b128 v[238:241], v20 offset:36976
	s_waitcnt lgkmcnt(7)
	v_cmp_eq_f32_e32 vcc, v198, v8
	s_nop 1
	v_cndmask_b32_e32 v10, 0, v38, vcc
	v_cmp_gt_f32_e32 vcc, v198, v8
	s_nop 1
	v_cndmask_b32_e64 v10, v10, 1, vcc
	v_cmp_eq_f32_e32 vcc, v199, v8
	s_nop 1
	v_cndmask_b32_e32 v9, 0, v39, vcc
	v_cmp_gt_f32_e32 vcc, v199, v8
	s_nop 1
	v_cndmask_b32_e64 v9, v9, 1, vcc
	v_mov_b32_e32 v11, 1
	v_mov_b32_e32 v12, 1
	v_cmp_eq_f32_e32 vcc, v200, v8
	s_nop 1
	v_cndmask_b32_e32 v12, 0, v40, vcc
	v_cmp_gt_f32_e32 vcc, v200, v8
	s_nop 1
	v_cndmask_b32_e64 v12, v12, 1, vcc
	v_cmp_eq_f32_e32 vcc, v201, v8
	s_nop 1
	v_cndmask_b32_e32 v11, 0, v41, vcc
	v_cmp_gt_f32_e32 vcc, v201, v8
	s_nop 1
	v_cndmask_b32_e64 v11, v11, 1, vcc
	v_mov_b32_e32 v13, 1
	v_mov_b32_e32 v14, 1
	s_waitcnt lgkmcnt(6)
	v_cmp_eq_f32_e32 vcc, v202, v8
	s_nop 1
	v_cndmask_b32_e32 v14, 0, v42, vcc
	v_cmp_gt_f32_e32 vcc, v202, v8
	s_nop 1
	v_cndmask_b32_e64 v14, v14, 1, vcc
	v_cmp_eq_f32_e32 vcc, v203, v8
	s_nop 1
	v_cndmask_b32_e32 v13, 0, v43, vcc
	v_cmp_gt_f32_e32 vcc, v203, v8
	s_nop 1
	v_cndmask_b32_e64 v13, v13, 1, vcc
	v_mov_b32_e32 v15, 1
	v_mov_b32_e32 v16, 1
	v_cmp_eq_f32_e32 vcc, v204, v8
	s_nop 1
	v_cndmask_b32_e32 v16, 0, v44, vcc
	v_cmp_gt_f32_e32 vcc, v204, v8
	s_nop 1
	v_cndmask_b32_e64 v16, v16, 1, vcc
	v_cmp_eq_f32_e32 vcc, v205, v8
	s_nop 1
	v_cndmask_b32_e32 v15, 0, v45, vcc
	v_cmp_gt_f32_e32 vcc, v205, v8
	s_nop 1
	v_cndmask_b32_e64 v15, v15, 1, vcc
	v_mov_b32_e32 v17, 1
	v_mov_b32_e32 v25, 1
	s_waitcnt lgkmcnt(5)
	v_cmp_eq_f32_e32 vcc, v206, v8
	s_nop 1
	v_cndmask_b32_e32 v25, 0, v46, vcc
	v_cmp_gt_f32_e32 vcc, v206, v8
	s_nop 1
	v_cndmask_b32_e64 v25, v25, 1, vcc
	v_cmp_eq_f32_e32 vcc, v207, v8
	s_nop 1
	v_cndmask_b32_e32 v17, 0, v47, vcc
	v_cmp_gt_f32_e32 vcc, v207, v8
	s_nop 1
	v_cndmask_b32_e64 v17, v17, 1, vcc
	v_mov_b32_e32 v26, 1
	v_mov_b32_e32 v27, 1
	v_cmp_eq_f32_e32 vcc, v208, v8
	s_nop 1
	v_cndmask_b32_e32 v27, 0, v48, vcc
	v_cmp_gt_f32_e32 vcc, v208, v8
	s_nop 1
	v_cndmask_b32_e64 v27, v27, 1, vcc
	v_cmp_eq_f32_e32 vcc, v209, v8
	s_nop 1
	v_cndmask_b32_e32 v26, 0, v49, vcc
	v_cmp_gt_f32_e32 vcc, v209, v8
	s_nop 1
	v_cndmask_b32_e64 v26, v26, 1, vcc
	v_mov_b32_e32 v28, 1
	v_mov_b32_e32 v29, 1
	s_waitcnt lgkmcnt(4)
	v_cmp_eq_f32_e32 vcc, v218, v8
	s_nop 1
	v_cndmask_b32_e32 v29, 0, v50, vcc
	v_cmp_gt_f32_e32 vcc, v218, v8
	s_nop 1
	v_cndmask_b32_e64 v29, v29, 1, vcc
	v_cmp_eq_f32_e32 vcc, v219, v8
	s_nop 1
	v_cndmask_b32_e32 v28, 0, v51, vcc
	v_cmp_gt_f32_e32 vcc, v219, v8
	s_nop 1
	v_cndmask_b32_e64 v28, v28, 1, vcc
	v_mov_b32_e32 v30, 1
	v_mov_b32_e32 v31, 1
	v_cmp_eq_f32_e32 vcc, v220, v8
	s_nop 1
	v_cndmask_b32_e32 v31, 0, v52, vcc
	v_cmp_gt_f32_e32 vcc, v220, v8
	s_nop 1
	v_cndmask_b32_e64 v31, v31, 1, vcc
	v_cmp_eq_f32_e32 vcc, v221, v8
	s_nop 1
	v_cndmask_b32_e32 v30, 0, v53, vcc
	v_cmp_gt_f32_e32 vcc, v221, v8
	s_nop 1
	v_cndmask_b32_e64 v30, v30, 1, vcc
	v_mov_b32_e32 v32, 1
	v_mov_b32_e32 v33, 1
	s_waitcnt lgkmcnt(3)
	v_cmp_eq_f32_e32 vcc, v222, v8
	s_nop 1
	v_cndmask_b32_e32 v33, 0, v54, vcc
	v_cmp_gt_f32_e32 vcc, v222, v8
	s_nop 1
	v_cndmask_b32_e64 v33, v33, 1, vcc
	v_cmp_eq_f32_e32 vcc, v223, v8
	s_nop 1
	v_cndmask_b32_e32 v32, 0, v55, vcc
	v_cmp_gt_f32_e32 vcc, v223, v8
	s_nop 1
	v_cndmask_b32_e64 v32, v32, 1, vcc
	v_mov_b32_e32 v95, 1
	v_mov_b32_e32 v96, 1
	v_cmp_eq_f32_e32 vcc, v224, v8
	s_nop 1
	v_cndmask_b32_e32 v96, 0, v57, vcc
	v_cmp_gt_f32_e32 vcc, v224, v8
	s_nop 1
	v_cndmask_b32_e64 v96, v96, 1, vcc
	v_cmp_eq_f32_e32 vcc, v225, v8
	s_nop 1
	v_cndmask_b32_e32 v95, 0, v58, vcc
	v_cmp_gt_f32_e32 vcc, v225, v8
	s_nop 1
	v_cndmask_b32_e64 v95, v95, 1, vcc
	v_mov_b32_e32 v97, 1
	v_mov_b32_e32 v98, 1
	s_waitcnt lgkmcnt(2)
	v_cmp_eq_f32_e32 vcc, v226, v8
	s_nop 1
	v_cndmask_b32_e32 v98, 0, v59, vcc
	v_cmp_gt_f32_e32 vcc, v226, v8
	s_nop 1
	v_cndmask_b32_e64 v98, v98, 1, vcc
	v_cmp_eq_f32_e32 vcc, v227, v8
	s_nop 1
	v_cndmask_b32_e32 v97, 0, v60, vcc
	v_cmp_gt_f32_e32 vcc, v227, v8
	s_nop 1
	v_cndmask_b32_e64 v97, v97, 1, vcc
	v_mov_b32_e32 v99, 1
	v_mov_b32_e32 v100, 1
	v_cmp_eq_f32_e32 vcc, v228, v8
	s_nop 1
	v_cndmask_b32_e32 v100, 0, v61, vcc
	v_cmp_gt_f32_e32 vcc, v228, v8
	s_nop 1
	v_cndmask_b32_e64 v100, v100, 1, vcc
	v_cmp_eq_f32_e32 vcc, v229, v8
	s_nop 1
	v_cndmask_b32_e32 v99, 0, v62, vcc
	v_cmp_gt_f32_e32 vcc, v229, v8
	s_nop 1
	v_cndmask_b32_e64 v99, v99, 1, vcc
	v_mov_b32_e32 v101, 1
	v_mov_b32_e32 v102, 1
	s_waitcnt lgkmcnt(1)
	v_cmp_eq_f32_e32 vcc, v230, v8
	s_nop 1
	v_cndmask_b32_e32 v102, 0, v63, vcc
	v_cmp_gt_f32_e32 vcc, v230, v8
	s_nop 1
	v_cndmask_b32_e64 v102, v102, 1, vcc
	v_cmp_eq_f32_e32 vcc, v231, v8
	s_nop 1
	v_cndmask_b32_e32 v101, 0, v64, vcc
	v_cmp_gt_f32_e32 vcc, v231, v8
	s_nop 1
	v_cndmask_b32_e64 v101, v101, 1, vcc
	v_mov_b32_e32 v103, 1
	v_mov_b32_e32 v104, 1
	v_cmp_eq_f32_e32 vcc, v232, v8
	s_nop 1
	v_cndmask_b32_e32 v104, 0, v65, vcc
	v_cmp_gt_f32_e32 vcc, v232, v8
	s_nop 1
	v_cndmask_b32_e64 v104, v104, 1, vcc
	v_cmp_eq_f32_e32 vcc, v233, v8
	s_nop 1
	v_cndmask_b32_e32 v103, 0, v66, vcc
	v_cmp_gt_f32_e32 vcc, v233, v8
	s_nop 1
	v_cndmask_b32_e64 v103, v103, 1, vcc
	v_mov_b32_e32 v105, 1
	v_mov_b32_e32 v106, 1
	s_waitcnt lgkmcnt(0)
	v_cmp_eq_f32_e32 vcc, v238, v8
	s_nop 1
	v_cndmask_b32_e32 v106, 0, v67, vcc
	v_cmp_gt_f32_e32 vcc, v238, v8
	s_nop 1
	v_cndmask_b32_e64 v106, v106, 1, vcc
	v_cmp_eq_f32_e32 vcc, v239, v8
	s_nop 1
	v_cndmask_b32_e32 v105, 0, v68, vcc
	v_cmp_gt_f32_e32 vcc, v239, v8
	s_nop 1
	v_cndmask_b32_e64 v105, v105, 1, vcc
	v_mov_b32_e32 v2, 1
	v_cmp_eq_f32_e32 vcc, v240, v8
	s_nop 1
	v_cndmask_b32_e32 v2, 0, v69, vcc
	v_cmp_gt_f32_e32 vcc, v240, v8
	s_nop 1
	v_cndmask_b32_e64 v2, v2, 1, vcc
	v_add3_u32 v3, v9, v10, v12
	v_add3_u32 v3, v3, v11, v14
	v_add3_u32 v3, v3, v13, v16
	v_add3_u32 v3, v3, v15, v25
	v_add3_u32 v3, v3, v17, v27
	v_add3_u32 v3, v3, v26, v29
	v_add3_u32 v3, v3, v28, v31
	v_add3_u32 v3, v3, v30, v33
	v_add3_u32 v3, v3, v32, v96
	v_add3_u32 v3, v3, v95, v98
	v_add3_u32 v3, v3, v97, v100
	v_add3_u32 v3, v3, v99, v102
	v_add3_u32 v3, v3, v101, v104
	v_cmp_gt_f32_e32 vcc, v241, v8
	s_nop 1
	v_addc_co_u32_e32 v3, vcc, v3, v103, vcc
	v_add_u32_e32 v3, v3, v106
	v_add3_u32 v3, v3, v105, v2
	v_cmp_gt_u32_e32 vcc, 4, v3
	s_and_saveexec_b64 s[8:9], vcc
	v_lshl_add_u32 v2, v3, 2, v22
	ds_write_b32 v2, v8 offset:40960
	s_or_b64 exec, exec, s[8:9]
	v_mov_b32_e32 v4, v240
	v_mov_b32_e32 v5, v241
	s_waitcnt lgkmcnt(0)
	v_add_u32_e32 v2, s28, v34
	s_and_saveexec_b64 s[8:9], vcc
	s_cbranch_execz .LBB0_965
	ds_read_b128 v[10:13], v22 offset:40960
	s_waitcnt lgkmcnt(0)
	v_sub_f32_e32 v9, v11, v10
	v_sub_f32_e32 v5, v12, v10
	v_mul_f32_e32 v9, 0x3fb8aa3b, v9
	v_sub_f32_e32 v4, v13, v10
	v_mul_f32_e32 v5, 0x3fb8aa3b, v5
	v_exp_f32_e32 v9, v9
	v_mul_f32_e32 v4, 0x3fb8aa3b, v4
	v_exp_f32_e32 v5, v5
	v_exp_f32_e32 v4, v4
	v_add_f32_e32 v9, 1.0, v9
	v_add_f32_e32 v5, v5, v9
	v_add_f32_e32 v4, v4, v5
	v_div_scale_f32 v5, s[24:25], v4, v4, 1.0
	v_rcp_f32_e32 v9, v5
	v_div_scale_f32 v11, vcc, 1.0, v4, 1.0
	v_fma_f32 v12, -v5, v9, 1.0
	v_fmac_f32_e32 v9, v12, v9
	v_mul_f32_e32 v12, v11, v9
	v_fma_f32 v13, -v5, v12, v11
	v_fmac_f32_e32 v12, v13, v9
	v_fma_f32 v5, -v5, v12, v11
	v_div_fmas_f32 v5, v5, v9, v12
	v_div_fixup_f32 v11, v5, v4, 1.0
	v_lshl_or_b32 v4, v2, 2, v3
	v_sub_f32_e32 v3, v8, v10
	v_mul_f32_e32 v3, 0x3fb8aa3b, v3
	v_exp_f32_e32 v3, v3
	v_ashrrev_i32_e32 v5, 31, v4
	v_lshlrev_b64 v[4:5], 2, v[4:5]
	v_lshl_add_u64 v[8:9], s[16:17], 0, v[4:5]
	v_mul_f32_e32 v3, v3, v11
	v_lshl_add_u64 v[4:5], s[18:19], 0, v[4:5]
	global_store_dword v[8:9], v21, off
	global_store_dword v[4:5], v3, off
	ds_add_u32 v35, v83 offset:33792

.LBB0_967:
	s_or_b64 exec, exec, s[8:9]
	s_waitcnt lgkmcnt(0)
	ds_read2_b32 v[2:3], v6 offset0:2 offset1:34
	ds_read_b32 v4, v84
	ds_read_b32 v7, v85
	ds_read_b32 v8, v86
	ds_read_b32 v9, v87
	ds_read_b32 v10, v88
	ds_read_b32 v11, v89
	ds_read_b32 v12, v90
	ds_read_b32 v13, v91
	s_waitcnt lgkmcnt(7)
	v_add_f32_e32 v14, 0, v4
	ds_read2_b32 v[4:5], v6 offset0:66 offset1:98
	s_waitcnt lgkmcnt(7)
	v_add_f32_e32 v14, v14, v7
	v_add_f32_e32 v2, 0, v2
	v_add_f32_e32 v15, v2, v3
	ds_read2_b32 v[2:3], v6 offset0:130 offset1:162
	ds_read2_b32 v[6:7], v6 offset0:194 offset1:226
	s_waitcnt lgkmcnt(2)
	v_add_f32_e32 v4, v15, v4
	v_add_f32_e32 v4, v4, v5
	s_waitcnt lgkmcnt(1)
	v_add_f32_e32 v2, v4, v2
	v_add_f32_e32 v2, v2, v3
	s_waitcnt lgkmcnt(0)
	v_add_f32_e32 v2, v2, v6
	v_add_f32_e32 v2, v2, v7
	v_fmamk_f32 v2, v2, 0x3a000000, v81
	v_mul_f32_e32 v3, 0x4f800000, v2
	v_cmp_gt_f32_e32 vcc, s26, v2
	v_add_f32_e32 v4, v14, v8
	v_add_f32_e32 v4, v4, v9
	v_cndmask_b32_e32 v2, v2, v3, vcc
	v_sqrt_f32_e32 v3, v2
	v_add_f32_e32 v4, v4, v10
	v_add_f32_e32 v4, v4, v11
	v_add_f32_e32 v4, v4, v12
	v_add_u32_e32 v5, -1, v3
	v_fma_f32 v6, -v5, v3, v2
	v_cmp_ge_f32_e64 s[8:9], 0, v6
	v_add_u32_e32 v6, 1, v3
	v_add_f32_e32 v4, v4, v13
	v_cndmask_b32_e64 v5, v3, v5, s[8:9]
	v_fma_f32 v3, -v6, v3, v2
	v_cmp_lt_f32_e64 s[8:9], 0, v3
	v_mov_b32_e32 v9, 1
	s_nop 0
	v_cndmask_b32_e64 v3, v5, v6, s[8:9]
	v_mul_f32_e32 v5, 0x37800000, v3
	v_cndmask_b32_e32 v3, v3, v5, vcc
	v_cmp_class_f32_e32 vcc, v2, v82
	s_nop 1
	v_cndmask_b32_e32 v2, v3, v2, vcc
	v_div_scale_f32 v3, s[8:9], v2, v2, 1.0
	v_rcp_f32_e32 v5, v3
	s_nop 0
	v_fma_f32 v6, -v3, v5, 1.0
	v_fmac_f32_e32 v5, v6, v5
	v_div_scale_f32 v6, vcc, 1.0, v2, 1.0
	v_mul_f32_e32 v7, v6, v5
	v_fma_f32 v8, -v3, v7, v6
	v_fmac_f32_e32 v7, v8, v5
	v_fma_f32 v3, -v3, v7, v6
	v_div_fmas_f32 v3, v3, v5, v7
	v_div_fixup_f32 v6, v3, v2, 1.0
	v_fma_f32 v2, v4, v6, v56
	v_cmp_o_f32_e32 vcc, v2, v2
	v_mov_b32_e32 v8, 1
	s_nop 0
	v_cndmask_b32_e32 v7, v94, v2, vcc
	ds_write_b32 v71, v7 offset:36864
	s_waitcnt lgkmcnt(0)
	ds_read_b128 v[198:201], v20 offset:36864
	ds_read_b128 v[202:205], v20 offset:36880
	ds_read_b128 v[206:209], v20 offset:36896
	ds_read_b128 v[218:221], v20 offset:36912
	ds_read_b128 v[222:225], v20 offset:36928
	ds_read_b128 v[226:229], v20 offset:36944
	ds_read_b128 v[230:233], v20 offset:36960
	ds_read_b128 v[238:241], v20 offset:36976
	s_waitcnt lgkmcnt(7)
	v_cmp_eq_f32_e32 vcc, v198, v7
	s_nop 1
	v_cndmask_b32_e32 v9, 0, v38, vcc
	v_cmp_gt_f32_e32 vcc, v198, v7
	s_nop 1
	v_cndmask_b32_e64 v9, v9, 1, vcc
	v_cmp_eq_f32_e32 vcc, v199, v7
	s_nop 1
	v_cndmask_b32_e32 v8, 0, v39, vcc
	v_cmp_gt_f32_e32 vcc, v199, v7
	s_nop 1
	v_cndmask_b32_e64 v8, v8, 1, vcc
	v_mov_b32_e32 v10, 1
	v_mov_b32_e32 v11, 1
	v_cmp_eq_f32_e32 vcc, v200, v7
	s_nop 1
	v_cndmask_b32_e32 v11, 0, v40, vcc
	v_cmp_gt_f32_e32 vcc, v200, v7
	s_nop 1
	v_cndmask_b32_e64 v11, v11, 1, vcc
	v_cmp_eq_f32_e32 vcc, v201, v7
	s_nop 1
	v_cndmask_b32_e32 v10, 0, v41, vcc
	v_cmp_gt_f32_e32 vcc, v201, v7
	s_nop 1
	v_cndmask_b32_e64 v10, v10, 1, vcc
	v_mov_b32_e32 v12, 1
	v_mov_b32_e32 v13, 1
	s_waitcnt lgkmcnt(6)
	v_cmp_eq_f32_e32 vcc, v202, v7
	s_nop 1
	v_cndmask_b32_e32 v13, 0, v42, vcc
	v_cmp_gt_f32_e32 vcc, v202, v7
	s_nop 1
	v_cndmask_b32_e64 v13, v13, 1, vcc
	v_cmp_eq_f32_e32 vcc, v203, v7
	s_nop 1
	v_cndmask_b32_e32 v12, 0, v43, vcc
	v_cmp_gt_f32_e32 vcc, v203, v7
	s_nop 1
	v_cndmask_b32_e64 v12, v12, 1, vcc
	v_mov_b32_e32 v14, 1
	v_mov_b32_e32 v15, 1
	v_cmp_eq_f32_e32 vcc, v204, v7
	s_nop 1
	v_cndmask_b32_e32 v15, 0, v44, vcc
	v_cmp_gt_f32_e32 vcc, v204, v7
	s_nop 1
	v_cndmask_b32_e64 v15, v15, 1, vcc
	v_cmp_eq_f32_e32 vcc, v205, v7
	s_nop 1
	v_cndmask_b32_e32 v14, 0, v45, vcc
	v_cmp_gt_f32_e32 vcc, v205, v7
	s_nop 1
	v_cndmask_b32_e64 v14, v14, 1, vcc
	v_mov_b32_e32 v16, 1
	v_mov_b32_e32 v17, 1
	s_waitcnt lgkmcnt(5)
	v_cmp_eq_f32_e32 vcc, v206, v7
	s_nop 1
	v_cndmask_b32_e32 v17, 0, v46, vcc
	v_cmp_gt_f32_e32 vcc, v206, v7
	s_nop 1
	v_cndmask_b32_e64 v17, v17, 1, vcc
	v_cmp_eq_f32_e32 vcc, v207, v7
	s_nop 1
	v_cndmask_b32_e32 v16, 0, v47, vcc
	v_cmp_gt_f32_e32 vcc, v207, v7
	s_nop 1
	v_cndmask_b32_e64 v16, v16, 1, vcc
	v_mov_b32_e32 v25, 1
	v_mov_b32_e32 v26, 1
	v_cmp_eq_f32_e32 vcc, v208, v7
	s_nop 1
	v_cndmask_b32_e32 v26, 0, v48, vcc
	v_cmp_gt_f32_e32 vcc, v208, v7
	s_nop 1
	v_cndmask_b32_e64 v26, v26, 1, vcc
	v_cmp_eq_f32_e32 vcc, v209, v7
	s_nop 1
	v_cndmask_b32_e32 v25, 0, v49, vcc
	v_cmp_gt_f32_e32 vcc, v209, v7
	s_nop 1
	v_cndmask_b32_e64 v25, v25, 1, vcc
	v_mov_b32_e32 v27, 1
	v_mov_b32_e32 v28, 1
	s_waitcnt lgkmcnt(4)
	v_cmp_eq_f32_e32 vcc, v218, v7
	s_nop 1
	v_cndmask_b32_e32 v28, 0, v50, vcc
	v_cmp_gt_f32_e32 vcc, v218, v7
	s_nop 1
	v_cndmask_b32_e64 v28, v28, 1, vcc
	v_cmp_eq_f32_e32 vcc, v219, v7
	s_nop 1
	v_cndmask_b32_e32 v27, 0, v51, vcc
	v_cmp_gt_f32_e32 vcc, v219, v7
	s_nop 1
	v_cndmask_b32_e64 v27, v27, 1, vcc
	v_mov_b32_e32 v29, 1
	v_mov_b32_e32 v30, 1
	v_cmp_eq_f32_e32 vcc, v220, v7
	s_nop 1
	v_cndmask_b32_e32 v30, 0, v52, vcc
	v_cmp_gt_f32_e32 vcc, v220, v7
	s_nop 1
	v_cndmask_b32_e64 v30, v30, 1, vcc
	v_cmp_eq_f32_e32 vcc, v221, v7
	s_nop 1
	v_cndmask_b32_e32 v29, 0, v53, vcc
	v_cmp_gt_f32_e32 vcc, v221, v7
	s_nop 1
	v_cndmask_b32_e64 v29, v29, 1, vcc
	v_mov_b32_e32 v31, 1
	v_mov_b32_e32 v32, 1
	s_waitcnt lgkmcnt(3)
	v_cmp_eq_f32_e32 vcc, v222, v7
	s_nop 1
	v_cndmask_b32_e32 v32, 0, v54, vcc
	v_cmp_gt_f32_e32 vcc, v222, v7
	s_nop 1
	v_cndmask_b32_e64 v32, v32, 1, vcc
	v_cmp_eq_f32_e32 vcc, v223, v7
	s_nop 1
	v_cndmask_b32_e32 v31, 0, v55, vcc
	v_cmp_gt_f32_e32 vcc, v223, v7
	s_nop 1
	v_cndmask_b32_e64 v31, v31, 1, vcc
	v_mov_b32_e32 v33, 1
	v_mov_b32_e32 v95, 1
	v_cmp_eq_f32_e32 vcc, v224, v7
	s_nop 1
	v_cndmask_b32_e32 v95, 0, v57, vcc
	v_cmp_gt_f32_e32 vcc, v224, v7
	s_nop 1
	v_cndmask_b32_e64 v95, v95, 1, vcc
	v_cmp_eq_f32_e32 vcc, v225, v7
	s_nop 1
	v_cndmask_b32_e32 v33, 0, v58, vcc
	v_cmp_gt_f32_e32 vcc, v225, v7
	s_nop 1
	v_cndmask_b32_e64 v33, v33, 1, vcc
	v_mov_b32_e32 v96, 1
	v_mov_b32_e32 v97, 1
	s_waitcnt lgkmcnt(2)
	v_cmp_eq_f32_e32 vcc, v226, v7
	s_nop 1
	v_cndmask_b32_e32 v97, 0, v59, vcc
	v_cmp_gt_f32_e32 vcc, v226, v7
	s_nop 1
	v_cndmask_b32_e64 v97, v97, 1, vcc
	v_cmp_eq_f32_e32 vcc, v227, v7
	s_nop 1
	v_cndmask_b32_e32 v96, 0, v60, vcc
	v_cmp_gt_f32_e32 vcc, v227, v7
	s_nop 1
	v_cndmask_b32_e64 v96, v96, 1, vcc
	v_mov_b32_e32 v98, 1
	v_mov_b32_e32 v99, 1
	v_cmp_eq_f32_e32 vcc, v228, v7
	s_nop 1
	v_cndmask_b32_e32 v99, 0, v61, vcc
	v_cmp_gt_f32_e32 vcc, v228, v7
	s_nop 1
	v_cndmask_b32_e64 v99, v99, 1, vcc
	v_cmp_eq_f32_e32 vcc, v229, v7
	s_nop 1
	v_cndmask_b32_e32 v98, 0, v62, vcc
	v_cmp_gt_f32_e32 vcc, v229, v7
	s_nop 1
	v_cndmask_b32_e64 v98, v98, 1, vcc
	v_mov_b32_e32 v100, 1
	v_mov_b32_e32 v101, 1
	s_waitcnt lgkmcnt(1)
	v_cmp_eq_f32_e32 vcc, v230, v7
	s_nop 1
	v_cndmask_b32_e32 v101, 0, v63, vcc
	v_cmp_gt_f32_e32 vcc, v230, v7
	s_nop 1
	v_cndmask_b32_e64 v101, v101, 1, vcc
	v_cmp_eq_f32_e32 vcc, v231, v7
	s_nop 1
	v_cndmask_b32_e32 v100, 0, v64, vcc
	v_cmp_gt_f32_e32 vcc, v231, v7
	s_nop 1
	v_cndmask_b32_e64 v100, v100, 1, vcc
	v_mov_b32_e32 v102, 1
	v_mov_b32_e32 v103, 1
	v_cmp_eq_f32_e32 vcc, v232, v7
	s_nop 1
	v_cndmask_b32_e32 v103, 0, v65, vcc
	v_cmp_gt_f32_e32 vcc, v232, v7
	s_nop 1
	v_cndmask_b32_e64 v103, v103, 1, vcc
	v_cmp_eq_f32_e32 vcc, v233, v7
	s_nop 1
	v_cndmask_b32_e32 v102, 0, v66, vcc
	v_cmp_gt_f32_e32 vcc, v233, v7
	s_nop 1
	v_cndmask_b32_e64 v102, v102, 1, vcc
	v_mov_b32_e32 v104, 1
	v_mov_b32_e32 v105, 1
	s_waitcnt lgkmcnt(0)
	v_cmp_eq_f32_e32 vcc, v238, v7
	s_nop 1
	v_cndmask_b32_e32 v105, 0, v67, vcc
	v_cmp_gt_f32_e32 vcc, v238, v7
	s_nop 1
	v_cndmask_b32_e64 v105, v105, 1, vcc
	v_cmp_eq_f32_e32 vcc, v239, v7
	s_nop 1
	v_cndmask_b32_e32 v104, 0, v68, vcc
	v_cmp_gt_f32_e32 vcc, v239, v7
	s_nop 1
	v_cndmask_b32_e64 v104, v104, 1, vcc
	v_mov_b32_e32 v2, 1
	v_cmp_eq_f32_e32 vcc, v240, v7
	s_nop 1
	v_cndmask_b32_e32 v2, 0, v69, vcc
	v_cmp_gt_f32_e32 vcc, v240, v7
	s_nop 1
	v_cndmask_b32_e64 v2, v2, 1, vcc
	v_add3_u32 v3, v8, v9, v11
	v_add3_u32 v3, v3, v10, v13
	v_add3_u32 v3, v3, v12, v15
	v_add3_u32 v3, v3, v14, v17
	v_add3_u32 v3, v3, v16, v26
	v_add3_u32 v3, v3, v25, v28
	v_add3_u32 v3, v3, v27, v30
	v_add3_u32 v3, v3, v29, v32
	v_add3_u32 v3, v3, v31, v95
	v_add3_u32 v3, v3, v33, v97
	v_add3_u32 v3, v3, v96, v99
	v_add3_u32 v3, v3, v98, v101
	v_add3_u32 v3, v3, v100, v103
	v_cmp_gt_f32_e32 vcc, v241, v7
	s_nop 1
	v_addc_co_u32_e32 v3, vcc, v3, v102, vcc
	v_add_u32_e32 v3, v3, v105
	v_add3_u32 v3, v3, v104, v2
	v_cmp_gt_u32_e32 vcc, 4, v3
	s_and_saveexec_b64 s[8:9], vcc
	v_lshl_add_u32 v2, v3, 2, v22
	ds_write_b32 v2, v7 offset:40960
	s_or_b64 exec, exec, s[8:9]
	v_mov_b32_e32 v4, v240
	v_mov_b32_e32 v5, v241
	s_waitcnt lgkmcnt(0)
	v_add_u32_e32 v2, s28, v70
	s_and_saveexec_b64 s[8:9], vcc
	s_cbranch_execz .LBB0_1095
	ds_read_b128 v[8:11], v22 offset:40960
	s_waitcnt lgkmcnt(0)
	v_sub_f32_e32 v9, v9, v8
	v_sub_f32_e32 v5, v10, v8
	v_mul_f32_e32 v9, 0x3fb8aa3b, v9
	v_sub_f32_e32 v4, v11, v8
	v_mul_f32_e32 v5, 0x3fb8aa3b, v5
	v_exp_f32_e32 v9, v9
	v_mul_f32_e32 v4, 0x3fb8aa3b, v4
	v_exp_f32_e32 v5, v5
	v_exp_f32_e32 v4, v4
	v_add_f32_e32 v9, 1.0, v9
	v_add_f32_e32 v5, v5, v9
	v_add_f32_e32 v4, v4, v5
	v_div_scale_f32 v5, s[24:25], v4, v4, 1.0
	v_rcp_f32_e32 v9, v5
	v_div_scale_f32 v10, vcc, 1.0, v4, 1.0
	v_fma_f32 v11, -v5, v9, 1.0
	v_fmac_f32_e32 v9, v11, v9
	v_mul_f32_e32 v11, v10, v9
	v_fma_f32 v12, -v5, v11, v10
	v_fmac_f32_e32 v11, v12, v9
	v_fma_f32 v5, -v5, v11, v10
	v_div_fmas_f32 v5, v5, v9, v11
	v_div_fixup_f32 v10, v5, v4, 1.0
	v_lshl_or_b32 v4, v2, 2, v3
	v_sub_f32_e32 v3, v7, v8
	v_mul_f32_e32 v3, 0x3fb8aa3b, v3
	v_exp_f32_e32 v3, v3
	v_ashrrev_i32_e32 v5, 31, v4
	v_lshlrev_b64 v[4:5], 2, v[4:5]
	v_lshl_add_u64 v[8:9], s[16:17], 0, v[4:5]
	v_mul_f32_e32 v3, v3, v10
	v_lshl_add_u64 v[4:5], s[18:19], 0, v[4:5]
	global_store_dword v[8:9], v21, off
	global_store_dword v[4:5], v3, off
	ds_add_u32 v35, v83 offset:33792
